# prologue weight transposes: all 32 loads of a tile in flight (two 16-load iterations flattened on renamed registers)
# baseline (speedup 1.0000x reference)
.LBB0_30:
	s_lshl_b32 s13, s1, 1
	s_lshl_b32 s69, s7, 1
	v_or_b32_e32 v8, s13, v1
	v_or_b32_e32 v33, s69, v6
	s_add_i32 s72, s13, 4
	s_add_i32 s73, s69, 4
	s_add_i32 s74, s13, 8
	s_add_i32 s75, s69, 8
	s_add_i32 s76, s13, 12
	s_add_i32 s77, s69, 12
	s_add_i32 s78, s13, 16
	s_add_i32 s79, s69, 16
	s_add_i32 s80, s13, 20
	s_add_i32 s81, s69, 20
	s_add_i32 s82, s13, 24
	s_add_i32 s83, s69, 24
	s_add_i32 s13, s13, 28
	s_add_i32 s69, s69, 28
	v_mad_u64_u32 v[42:43], s[70:71], v33, s66, v[34:35]
	v_or_b32_e32 v74, s72, v1
	v_or_b32_e32 v75, s73, v6
	v_or_b32_e32 v76, s74, v1
	v_or_b32_e32 v77, s75, v6
	v_or_b32_e32 v78, s76, v1
	v_or_b32_e32 v79, s77, v6
	v_or_b32_e32 v80, s78, v1
	v_or_b32_e32 v81, s79, v6
	v_or_b32_e32 v82, s80, v1
	v_or_b32_e32 v83, s81, v6
	v_or_b32_e32 v84, s82, v1
	v_or_b32_e32 v85, s83, v6
	v_or_b32_e32 v86, s13, v1
	v_or_b32_e32 v87, s69, v6
	v_mad_u64_u32 v[44:45], s[70:71], v8, s66, v[34:35]
	v_mad_u64_u32 v[46:47], s[70:71], v75, s66, v[34:35]
	v_mad_u64_u32 v[48:49], s[70:71], v74, s66, v[34:35]
	v_mad_u64_u32 v[50:51], s[70:71], v77, s66, v[34:35]
	v_mad_u64_u32 v[52:53], s[70:71], v76, s66, v[34:35]
	v_mad_u64_u32 v[54:55], s[70:71], v79, s66, v[34:35]
	v_mad_u64_u32 v[56:57], s[70:71], v78, s66, v[34:35]
	v_mad_u64_u32 v[58:59], s[70:71], v81, s66, v[34:35]
	v_mad_u64_u32 v[60:61], s[70:71], v80, s66, v[34:35]
	v_mad_u64_u32 v[62:63], s[70:71], v83, s66, v[34:35]
	v_mad_u64_u32 v[64:65], s[70:71], v82, s66, v[34:35]
	v_mad_u64_u32 v[66:67], s[70:71], v85, s66, v[34:35]
	v_mad_u64_u32 v[68:69], s[70:71], v84, s66, v[34:35]
	v_mad_u64_u32 v[70:71], s[70:71], v87, s66, v[34:35]
	v_mad_u64_u32 v[72:73], s[70:71], v86, s66, v[34:35]
	global_load_dword v88, v[42:43], off
	global_load_dword v89, v[44:45], off
	global_load_dword v90, v[46:47], off
	global_load_dword v91, v[48:49], off
	global_load_dword v92, v[50:51], off
	global_load_dword v93, v[52:53], off
	global_load_dword v94, v[54:55], off
	global_load_dword v95, v[56:57], off
	global_load_dword v96, v[58:59], off
	global_load_dword v97, v[60:61], off
	global_load_dword v98, v[62:63], off
	global_load_dword v99, v[64:65], off
	global_load_dword v100, v[66:67], off
	global_load_dword v101, v[68:69], off
	global_load_dword v102, v[70:71], off
	global_load_dword v103, v[72:73], off
	s_add_i32 s7, s7, 16
	s_add_i32 s1, s1, 16
	s_lshl_b32 s13, s1, 1
	s_lshl_b32 s69, s7, 1
	v_or_b32_e32 v136, s13, v1
	v_or_b32_e32 v137, s69, v6
	s_add_i32 s72, s13, 4
	s_add_i32 s73, s69, 4
	s_add_i32 s74, s13, 8
	s_add_i32 s75, s69, 8
	s_add_i32 s76, s13, 12
	s_add_i32 s77, s69, 12
	s_add_i32 s78, s13, 16
	s_add_i32 s79, s69, 16
	s_add_i32 s80, s13, 20
	s_add_i32 s81, s69, 20
	s_add_i32 s82, s13, 24
	s_add_i32 s83, s69, 24
	s_add_i32 s13, s13, 28
	s_add_i32 s69, s69, 28
	v_mad_u64_u32 v[104:105], s[70:71], v137, s66, v[34:35]
	v_or_b32_e32 v138, s72, v1
	v_or_b32_e32 v139, s73, v6
	v_or_b32_e32 v140, s74, v1
	v_or_b32_e32 v141, s75, v6
	v_or_b32_e32 v142, s76, v1
	v_or_b32_e32 v143, s77, v6
	v_or_b32_e32 v144, s78, v1
	v_or_b32_e32 v145, s79, v6
	v_or_b32_e32 v146, s80, v1
	v_or_b32_e32 v154, s81, v6
	v_or_b32_e32 v155, s82, v1
	v_or_b32_e32 v156, s83, v6
	v_or_b32_e32 v157, s13, v1
	v_or_b32_e32 v158, s69, v6
	v_mad_u64_u32 v[106:107], s[70:71], v136, s66, v[34:35]
	v_mad_u64_u32 v[108:109], s[70:71], v139, s66, v[34:35]
	v_mad_u64_u32 v[110:111], s[70:71], v138, s66, v[34:35]
	v_mad_u64_u32 v[112:113], s[70:71], v141, s66, v[34:35]
	v_mad_u64_u32 v[114:115], s[70:71], v140, s66, v[34:35]
	v_mad_u64_u32 v[116:117], s[70:71], v143, s66, v[34:35]
	v_mad_u64_u32 v[118:119], s[70:71], v142, s66, v[34:35]
	v_mad_u64_u32 v[120:121], s[70:71], v145, s66, v[34:35]
	v_mad_u64_u32 v[122:123], s[70:71], v144, s66, v[34:35]
	v_mad_u64_u32 v[124:125], s[70:71], v154, s66, v[34:35]
	v_mad_u64_u32 v[126:127], s[70:71], v146, s66, v[34:35]
	v_mad_u64_u32 v[128:129], s[70:71], v156, s66, v[34:35]
	v_mad_u64_u32 v[130:131], s[70:71], v155, s66, v[34:35]
	v_mad_u64_u32 v[132:133], s[70:71], v158, s66, v[34:35]
	v_mad_u64_u32 v[134:135], s[70:71], v157, s66, v[34:35]
	global_load_dword v159, v[104:105], off
	global_load_dword v160, v[106:107], off
	global_load_dword v161, v[108:109], off
	global_load_dword v162, v[110:111], off
	global_load_dword v163, v[112:113], off
	global_load_dword v164, v[114:115], off
	global_load_dword v165, v[116:117], off
	global_load_dword v166, v[118:119], off
	global_load_dword v167, v[120:121], off
	global_load_dword v168, v[122:123], off
	global_load_dword v169, v[124:125], off
	global_load_dword v170, v[126:127], off
	global_load_dword v171, v[128:129], off
	global_load_dword v172, v[130:131], off
	global_load_dword v173, v[132:133], off
	global_load_dword v174, v[134:135], off
	v_mad_u64_u32 v[42:43], s[70:71], v33, s31, v[12:13]
	v_mad_u64_u32 v[44:45], s[70:71], v8, s31, v[12:13]
	v_mad_u64_u32 v[46:47], s[70:71], v75, s31, v[12:13]
	v_mad_u64_u32 v[48:49], s[70:71], v74, s31, v[12:13]
	v_mad_u64_u32 v[50:51], s[70:71], v77, s31, v[12:13]
	v_mad_u64_u32 v[52:53], s[70:71], v76, s31, v[12:13]
	v_mad_u64_u32 v[54:55], s[70:71], v79, s31, v[12:13]
	v_mad_u64_u32 v[56:57], s[70:71], v78, s31, v[12:13]
	v_mad_u64_u32 v[58:59], s[70:71], v81, s31, v[12:13]
	v_mad_u64_u32 v[60:61], s[70:71], v80, s31, v[12:13]
	v_mad_u64_u32 v[62:63], s[70:71], v83, s31, v[12:13]
	v_mad_u64_u32 v[64:65], s[70:71], v82, s31, v[12:13]
	v_mad_u64_u32 v[66:67], s[70:71], v85, s31, v[12:13]
	v_mad_u64_u32 v[68:69], s[70:71], v84, s31, v[12:13]
	v_mad_u64_u32 v[70:71], s[70:71], v87, s31, v[12:13]
	v_mad_u64_u32 v[72:73], s[70:71], v86, s31, v[12:13]
	s_waitcnt vmcnt(31)
	ds_write_b32 v42, v88
	s_waitcnt vmcnt(30)
	ds_write_b32 v44, v89
	s_waitcnt vmcnt(29)
	ds_write_b32 v46, v90
	s_waitcnt vmcnt(28)
	ds_write_b32 v48, v91
	s_waitcnt vmcnt(27)
	ds_write_b32 v50, v92
	s_waitcnt vmcnt(26)
	ds_write_b32 v52, v93
	s_waitcnt vmcnt(25)
	ds_write_b32 v54, v94
	s_waitcnt vmcnt(24)
	ds_write_b32 v56, v95
	s_waitcnt vmcnt(23)
	ds_write_b32 v58, v96
	s_waitcnt vmcnt(22)
	ds_write_b32 v60, v97
	s_waitcnt vmcnt(21)
	ds_write_b32 v62, v98
	s_waitcnt vmcnt(20)
	ds_write_b32 v64, v99
	s_waitcnt vmcnt(19)
	ds_write_b32 v66, v100
	s_waitcnt vmcnt(18)
	ds_write_b32 v68, v101
	s_waitcnt vmcnt(17)
	ds_write_b32 v70, v102
	s_waitcnt vmcnt(16)
	ds_write_b32 v72, v103
	v_mad_u64_u32 v[104:105], s[70:71], v137, s31, v[12:13]
	v_mad_u64_u32 v[106:107], s[70:71], v136, s31, v[12:13]
	v_mad_u64_u32 v[108:109], s[70:71], v139, s31, v[12:13]
	v_mad_u64_u32 v[110:111], s[70:71], v138, s31, v[12:13]
	v_mad_u64_u32 v[112:113], s[70:71], v141, s31, v[12:13]
	v_mad_u64_u32 v[114:115], s[70:71], v140, s31, v[12:13]
	v_mad_u64_u32 v[116:117], s[70:71], v143, s31, v[12:13]
	v_mad_u64_u32 v[118:119], s[70:71], v142, s31, v[12:13]
	v_mad_u64_u32 v[120:121], s[70:71], v145, s31, v[12:13]
	v_mad_u64_u32 v[122:123], s[70:71], v144, s31, v[12:13]
	v_mad_u64_u32 v[124:125], s[70:71], v154, s31, v[12:13]
	v_mad_u64_u32 v[126:127], s[70:71], v146, s31, v[12:13]
	v_mad_u64_u32 v[128:129], s[70:71], v156, s31, v[12:13]
	v_mad_u64_u32 v[130:131], s[70:71], v155, s31, v[12:13]
	v_mad_u64_u32 v[132:133], s[70:71], v158, s31, v[12:13]
	v_mad_u64_u32 v[134:135], s[70:71], v157, s31, v[12:13]
	s_waitcnt vmcnt(15)
	ds_write_b32 v104, v159
	s_waitcnt vmcnt(14)
	ds_write_b32 v106, v160
	s_waitcnt vmcnt(13)
	ds_write_b32 v108, v161
	s_waitcnt vmcnt(12)
	ds_write_b32 v110, v162
	s_waitcnt vmcnt(11)
	ds_write_b32 v112, v163
	s_waitcnt vmcnt(10)
	ds_write_b32 v114, v164
	s_waitcnt vmcnt(9)
	ds_write_b32 v116, v165
	s_waitcnt vmcnt(8)
	ds_write_b32 v118, v166
	s_waitcnt vmcnt(7)
	ds_write_b32 v120, v167
	s_waitcnt vmcnt(6)
	ds_write_b32 v122, v168
	s_waitcnt vmcnt(5)
	ds_write_b32 v124, v169
	s_waitcnt vmcnt(4)
	ds_write_b32 v126, v170
	s_waitcnt vmcnt(3)
	ds_write_b32 v128, v171
	s_waitcnt vmcnt(2)
	ds_write_b32 v130, v172
	s_waitcnt vmcnt(1)
	ds_write_b32 v132, v173
	s_waitcnt vmcnt(0)
	ds_write_b32 v134, v174
	s_add_i32 s7, s7, 16
	s_add_i32 s1, s1, 16
	s_add_i32 s12, s12, -16
	s_add_i32 s12, s12, -16
	s_cmp_lg_u32 s12, 0
	s_waitcnt lgkmcnt(0)
	s_lshl_b64 s[12:13], s[2:3], 11
	s_add_u32 s1, s21, s12
	ds_read2_b32 v[34:35], v3 offset0:33 offset1:41
	ds_read2_b32 v[46:47], v3 offset1:8
	ds_read2_b32 v[48:49], v3 offset0:66 offset1:74
	ds_read2_b32 v[50:51], v3 offset0:99 offset1:107
	ds_read2_b32 v[52:53], v3 offset0:132 offset1:140
	ds_read2_b32 v[54:55], v3 offset0:165 offset1:173
	ds_read2_b32 v[56:57], v3 offset0:198 offset1:206
	ds_read2_b32 v[58:59], v3 offset0:231 offset1:239
	s_addc_u32 s2, s22, s13
	s_lshl_b32 s0, s0, 1
	s_add_u32 s0, s1, s0
	s_addc_u32 s1, s2, 0
	v_lshlrev_b32_e32 v8, 1, v14
	v_lshl_add_u64 v[60:61], s[0:1], 0, v[8:9]
	s_waitcnt lgkmcnt(6)
	v_cvt_pk_bf16_f32 v42, v46, v34
	s_waitcnt lgkmcnt(4)
	v_cvt_pk_bf16_f32 v43, v48, v50
	s_waitcnt lgkmcnt(2)
	v_cvt_pk_bf16_f32 v44, v52, v54
	s_waitcnt lgkmcnt(0)
	v_cvt_pk_bf16_f32 v45, v56, v58
	v_lshl_add_u64 v[62:63], v[60:61], 0, v[24:25]
	global_store_dwordx4 v[62:63], v[42:45], off
	v_readlane_b32 s76, v254, 7
	v_readlane_b32 s83, v254, 6
	v_cvt_pk_bf16_f32 v42, v47, v35
	v_cvt_pk_bf16_f32 v43, v49, v51
	v_cvt_pk_bf16_f32 v44, v53, v55
	v_cvt_pk_bf16_f32 v45, v57, v59
	ds_read2_b32 v[46:47], v3 offset0:49 offset1:57
	ds_read2_b32 v[48:49], v3 offset0:16 offset1:24
	ds_read2_b32 v[50:51], v3 offset0:82 offset1:90
	ds_read2_b32 v[52:53], v3 offset0:115 offset1:123
	ds_read2_b32 v[54:55], v3 offset0:148 offset1:156
	ds_read2_b32 v[56:57], v3 offset0:181 offset1:189
	ds_read2_b32 v[58:59], v3 offset0:214 offset1:222
	ds_read2_b32 v[62:63], v3 offset0:247 offset1:255
	v_lshl_add_u64 v[34:35], v[60:61], 0, v[26:27]
	global_store_dwordx4 v[34:35], v[42:45], off
	v_lshl_add_u64 v[34:35], v[60:61], 0, v[28:29]
	v_readlane_b32 s77, v254, 8
	s_waitcnt lgkmcnt(6)
	v_cvt_pk_bf16_f32 v42, v48, v46
	s_waitcnt lgkmcnt(4)
	v_cvt_pk_bf16_f32 v43, v50, v52
	s_waitcnt lgkmcnt(2)
	v_cvt_pk_bf16_f32 v44, v54, v56
	s_waitcnt lgkmcnt(0)
	v_cvt_pk_bf16_f32 v45, v58, v62
	global_store_dwordx4 v[34:35], v[42:45], off
	v_lshl_add_u64 v[34:35], v[60:61], 0, v[30:31]
	s_nop 0
	v_cvt_pk_bf16_f32 v42, v49, v47
	v_cvt_pk_bf16_f32 v43, v51, v53
	v_cvt_pk_bf16_f32 v44, v55, v57
	v_cvt_pk_bf16_f32 v45, v59, v63
	global_store_dwordx4 v[34:35], v[42:45], off
	s_waitcnt lgkmcnt(0)

.LBB0_35:
	s_lshl_b32 s13, s1, 1
	s_lshl_b32 s69, s7, 1
	v_or_b32_e32 v8, s69, v6
	s_add_i32 s72, s13, 4
	s_add_i32 s73, s69, 4
	v_mov_b32_e32 v45, v9
	s_add_i32 s75, s69, 8
	v_lshlrev_b64 v[60:61], 12, v[8:9]
	v_mad_u64_u32 v[62:63], s[70:71], v8, s31, v[12:13]
	v_or_b32_e32 v44, s72, v1
	v_or_b32_e32 v8, s73, v6
	v_mov_b32_e32 v43, v9
	v_or_b32_e32 v42, s13, v1
	s_add_i32 s77, s69, 12
	v_lshlrev_b64 v[64:65], 12, v[44:45]
	v_lshlrev_b64 v[66:67], 12, v[8:9]
	v_mad_u64_u32 v[68:69], s[70:71], v8, s31, v[12:13]
	v_or_b32_e32 v8, s75, v6
	s_add_i32 s74, s13, 8
	s_add_i32 s76, s13, 12
	s_add_i32 s79, s69, 16
	v_lshlrev_b64 v[58:59], 12, v[42:43]
	v_lshl_add_u64 v[60:61], v[34:35], 0, v[60:61]
	v_lshl_add_u64 v[64:65], v[34:35], 0, v[64:65]
	v_lshlrev_b64 v[82:83], 12, v[8:9]
	v_mad_u64_u32 v[84:85], s[70:71], v8, s31, v[12:13]
	v_or_b32_e32 v8, s77, v6
	v_mov_b32_e32 v47, v9
	v_mov_b32_e32 v49, v9
	s_add_i32 s78, s13, 16
	s_add_i32 s81, s69, 20
	v_or_b32_e32 v46, s74, v1
	v_or_b32_e32 v48, s76, v1
	v_lshl_add_u64 v[58:59], v[34:35], 0, v[58:59]
	v_lshl_add_u64 v[66:67], v[34:35], 0, v[66:67]
	global_load_dword v33, v[60:61], off
	global_load_dword v63, v[58:59], off
	global_load_dword v69, v[66:67], off
	global_load_dword v85, v[64:65], off
	v_lshlrev_b64 v[60:61], 12, v[8:9]
	v_mad_u64_u32 v[64:65], s[70:71], v8, s31, v[12:13]
	v_or_b32_e32 v8, s79, v6
	v_mov_b32_e32 v51, v9
	s_add_i32 s80, s13, 20
	s_add_i32 s83, s69, 24
	v_or_b32_e32 v50, s78, v1
	v_lshlrev_b64 v[70:71], 12, v[46:47]
	v_lshlrev_b64 v[72:73], 12, v[48:49]
	v_lshl_add_u64 v[58:59], v[34:35], 0, v[82:83]
	v_lshl_add_u64 v[60:61], v[34:35], 0, v[60:61]
	v_lshlrev_b64 v[66:67], 12, v[8:9]
	v_mad_u64_u32 v[82:83], s[70:71], v8, s31, v[12:13]
	v_or_b32_e32 v8, s81, v6
	v_mov_b32_e32 v53, v9
	s_add_i32 s69, s69, 28
	v_or_b32_e32 v52, s80, v1
	v_lshlrev_b64 v[74:75], 12, v[50:51]
	v_lshl_add_u64 v[70:71], v[34:35], 0, v[70:71]
	v_lshl_add_u64 v[72:73], v[34:35], 0, v[72:73]
	global_load_dword v65, v[58:59], off
	global_load_dword v83, v[70:71], off
	global_load_dword v86, v[60:61], off
	global_load_dword v87, v[72:73], off
	v_lshl_add_u64 v[58:59], v[34:35], 0, v[66:67]
	v_lshlrev_b64 v[60:61], 12, v[8:9]
	v_mad_u64_u32 v[66:67], s[70:71], v8, s31, v[12:13]
	v_or_b32_e32 v8, s83, v6
	s_add_i32 s82, s13, 24
	s_add_i32 s13, s13, 28
	v_lshlrev_b64 v[76:77], 12, v[52:53]
	v_lshl_add_u64 v[74:75], v[34:35], 0, v[74:75]
	v_lshl_add_u64 v[60:61], v[34:35], 0, v[60:61]
	v_lshlrev_b64 v[70:71], 12, v[8:9]
	v_mad_u64_u32 v[72:73], s[70:71], v8, s31, v[12:13]
	v_or_b32_e32 v8, s69, v6
	v_mov_b32_e32 v55, v9
	v_mov_b32_e32 v57, v9
	v_or_b32_e32 v54, s82, v1
	v_or_b32_e32 v56, s13, v1
	v_lshl_add_u64 v[76:77], v[34:35], 0, v[76:77]
	global_load_dword v67, v[58:59], off
	global_load_dword v73, v[74:75], off
	s_nop 0
	global_load_dword v74, v[60:61], off
	global_load_dword v75, v[76:77], off
	v_lshlrev_b64 v[60:61], 12, v[8:9]
	v_lshlrev_b64 v[78:79], 12, v[54:55]
	v_lshlrev_b64 v[80:81], 12, v[56:57]
	v_lshl_add_u64 v[58:59], v[34:35], 0, v[70:71]
	v_lshl_add_u64 v[60:61], v[34:35], 0, v[60:61]
	v_lshl_add_u64 v[78:79], v[34:35], 0, v[78:79]
	v_lshl_add_u64 v[80:81], v[34:35], 0, v[80:81]
	global_load_dword v70, v[58:59], off
	global_load_dword v71, v[78:79], off
	s_nop 0
	global_load_dword v60, v[60:61], off
	s_nop 0
	global_load_dword v61, v[80:81], off
	s_add_i32 s7, s7, 16
	s_add_i32 s1, s1, 16
	v_mov_b32_e32 v105, v9
	s_lshl_b32 s13, s1, 1
	s_lshl_b32 s69, s7, 1
	v_or_b32_e32 v104, s69, v6
	s_add_i32 s72, s13, 4
	s_add_i32 s73, s69, 4
	v_mov_b32_e32 v109, v105
	s_add_i32 s75, s69, 8
	v_lshlrev_b64 v[124:125], 12, v[104:105]
	v_mad_u64_u32 v[126:127], s[70:71], v104, s31, v[12:13]
	v_or_b32_e32 v108, s72, v1
	v_or_b32_e32 v104, s73, v6
	v_mov_b32_e32 v107, v105
	v_or_b32_e32 v106, s13, v1
	s_add_i32 s77, s69, 12
	v_lshlrev_b64 v[128:129], 12, v[108:109]
	v_lshlrev_b64 v[130:131], 12, v[104:105]
	v_mad_u64_u32 v[132:133], s[70:71], v104, s31, v[12:13]
	v_or_b32_e32 v104, s75, v6
	s_add_i32 s74, s13, 8
	s_add_i32 s76, s13, 12
	s_add_i32 s79, s69, 16
	v_lshlrev_b64 v[122:123], 12, v[106:107]
	v_lshl_add_u64 v[124:125], v[34:35], 0, v[124:125]
	v_lshl_add_u64 v[128:129], v[34:35], 0, v[128:129]
	v_lshlrev_b64 v[154:155], 12, v[104:105]
	v_mad_u64_u32 v[156:157], s[70:71], v104, s31, v[12:13]
	v_or_b32_e32 v104, s77, v6
	v_mov_b32_e32 v111, v105
	v_mov_b32_e32 v113, v105
	s_add_i32 s78, s13, 16
	s_add_i32 s81, s69, 20
	v_or_b32_e32 v110, s74, v1
	v_or_b32_e32 v112, s76, v1
	v_lshl_add_u64 v[122:123], v[34:35], 0, v[122:123]
	v_lshl_add_u64 v[130:131], v[34:35], 0, v[130:131]
	global_load_dword v146, v[124:125], off
	global_load_dword v127, v[122:123], off
	global_load_dword v133, v[130:131], off
	global_load_dword v157, v[128:129], off
	v_lshlrev_b64 v[124:125], 12, v[104:105]
	v_mad_u64_u32 v[128:129], s[70:71], v104, s31, v[12:13]
	v_or_b32_e32 v104, s79, v6
	v_mov_b32_e32 v115, v105
	s_add_i32 s80, s13, 20
	s_add_i32 s83, s69, 24
	v_or_b32_e32 v114, s78, v1
	v_lshlrev_b64 v[134:135], 12, v[110:111]
	v_lshlrev_b64 v[136:137], 12, v[112:113]
	v_lshl_add_u64 v[122:123], v[34:35], 0, v[154:155]
	v_lshl_add_u64 v[124:125], v[34:35], 0, v[124:125]
	v_lshlrev_b64 v[130:131], 12, v[104:105]
	v_mad_u64_u32 v[154:155], s[70:71], v104, s31, v[12:13]
	v_or_b32_e32 v104, s81, v6
	v_mov_b32_e32 v117, v105
	s_add_i32 s69, s69, 28
	v_or_b32_e32 v116, s80, v1
	v_lshlrev_b64 v[138:139], 12, v[114:115]
	v_lshl_add_u64 v[134:135], v[34:35], 0, v[134:135]
	v_lshl_add_u64 v[136:137], v[34:35], 0, v[136:137]
	global_load_dword v129, v[122:123], off
	global_load_dword v155, v[134:135], off
	global_load_dword v158, v[124:125], off
	global_load_dword v159, v[136:137], off
	v_lshl_add_u64 v[122:123], v[34:35], 0, v[130:131]
	v_lshlrev_b64 v[124:125], 12, v[104:105]
	v_mad_u64_u32 v[130:131], s[70:71], v104, s31, v[12:13]
	v_or_b32_e32 v104, s83, v6
	s_add_i32 s82, s13, 24
	s_add_i32 s13, s13, 28
	v_lshlrev_b64 v[140:141], 12, v[116:117]
	v_lshl_add_u64 v[138:139], v[34:35], 0, v[138:139]
	v_lshl_add_u64 v[124:125], v[34:35], 0, v[124:125]
	v_lshlrev_b64 v[134:135], 12, v[104:105]
	v_mad_u64_u32 v[136:137], s[70:71], v104, s31, v[12:13]
	v_or_b32_e32 v104, s69, v6
	v_mov_b32_e32 v119, v105
	v_mov_b32_e32 v121, v105
	v_or_b32_e32 v118, s82, v1
	v_or_b32_e32 v120, s13, v1
	v_lshl_add_u64 v[140:141], v[34:35], 0, v[140:141]
	global_load_dword v131, v[122:123], off
	global_load_dword v137, v[138:139], off
	s_nop 0
	global_load_dword v138, v[124:125], off
	global_load_dword v139, v[140:141], off
	v_lshlrev_b64 v[124:125], 12, v[104:105]
	v_lshlrev_b64 v[142:143], 12, v[118:119]
	v_lshlrev_b64 v[144:145], 12, v[120:121]
	v_lshl_add_u64 v[122:123], v[34:35], 0, v[134:135]
	v_lshl_add_u64 v[124:125], v[34:35], 0, v[124:125]
	v_lshl_add_u64 v[142:143], v[34:35], 0, v[142:143]
	v_lshl_add_u64 v[144:145], v[34:35], 0, v[144:145]
	global_load_dword v134, v[122:123], off
	global_load_dword v135, v[142:143], off
	s_nop 0
	global_load_dword v124, v[124:125], off
	s_nop 0
	global_load_dword v125, v[144:145], off
	v_mad_u64_u32 v[42:43], s[70:71], v42, s31, v[12:13]
	v_mad_u64_u32 v[44:45], s[70:71], v44, s31, v[12:13]
	v_mad_u64_u32 v[46:47], s[70:71], v46, s31, v[12:13]
	v_mad_u64_u32 v[48:49], s[70:71], v48, s31, v[12:13]
	v_mad_u64_u32 v[50:51], s[70:71], v50, s31, v[12:13]
	v_mad_u64_u32 v[52:53], s[70:71], v52, s31, v[12:13]
	v_mad_u64_u32 v[54:55], s[70:71], v54, s31, v[12:13]
	v_mad_u64_u32 v[56:57], s[70:71], v56, s31, v[12:13]
	v_mad_u64_u32 v[58:59], s[70:71], v8, s31, v[12:13]
	s_waitcnt vmcnt(31)
	ds_write_b32 v62, v33
	s_waitcnt vmcnt(30)
	ds_write_b32 v42, v63
	s_waitcnt vmcnt(29)
	ds_write_b32 v68, v69
	s_waitcnt vmcnt(28)
	ds_write_b32 v44, v85
	s_waitcnt vmcnt(27)
	ds_write_b32 v84, v65
	s_waitcnt vmcnt(26)
	ds_write_b32 v46, v83
	s_waitcnt vmcnt(25)
	ds_write_b32 v64, v86
	s_waitcnt vmcnt(24)
	ds_write_b32 v48, v87
	s_waitcnt vmcnt(23)
	ds_write_b32 v82, v67
	s_waitcnt vmcnt(22)
	ds_write_b32 v50, v73
	s_waitcnt vmcnt(21)
	ds_write_b32 v66, v74
	s_waitcnt vmcnt(20)
	ds_write_b32 v52, v75
	s_waitcnt vmcnt(19)
	ds_write_b32 v72, v70
	s_waitcnt vmcnt(18)
	ds_write_b32 v54, v71
	s_waitcnt vmcnt(17)
	ds_write_b32 v58, v60
	s_waitcnt vmcnt(16)
	ds_write_b32 v56, v61
	v_mad_u64_u32 v[106:107], s[70:71], v106, s31, v[12:13]
	v_mad_u64_u32 v[108:109], s[70:71], v108, s31, v[12:13]
	v_mad_u64_u32 v[110:111], s[70:71], v110, s31, v[12:13]
	v_mad_u64_u32 v[112:113], s[70:71], v112, s31, v[12:13]
	v_mad_u64_u32 v[114:115], s[70:71], v114, s31, v[12:13]
	v_mad_u64_u32 v[116:117], s[70:71], v116, s31, v[12:13]
	v_mad_u64_u32 v[118:119], s[70:71], v118, s31, v[12:13]
	v_mad_u64_u32 v[120:121], s[70:71], v120, s31, v[12:13]
	v_mad_u64_u32 v[122:123], s[70:71], v104, s31, v[12:13]
	s_waitcnt vmcnt(15)
	ds_write_b32 v126, v146
	s_waitcnt vmcnt(14)
	ds_write_b32 v106, v127
	s_waitcnt vmcnt(13)
	ds_write_b32 v132, v133
	s_waitcnt vmcnt(12)
	ds_write_b32 v108, v157
	s_waitcnt vmcnt(11)
	ds_write_b32 v156, v129
	s_waitcnt vmcnt(10)
	ds_write_b32 v110, v155
	s_waitcnt vmcnt(9)
	ds_write_b32 v128, v158
	s_waitcnt vmcnt(8)
	ds_write_b32 v112, v159
	s_waitcnt vmcnt(7)
	ds_write_b32 v154, v131
	s_waitcnt vmcnt(6)
	ds_write_b32 v114, v137
	s_waitcnt vmcnt(5)
	ds_write_b32 v130, v138
	s_waitcnt vmcnt(4)
	ds_write_b32 v116, v139
	s_waitcnt vmcnt(3)
	ds_write_b32 v136, v134
	s_waitcnt vmcnt(2)
	ds_write_b32 v118, v135
	s_waitcnt vmcnt(1)
	ds_write_b32 v122, v124
	s_waitcnt vmcnt(0)
	ds_write_b32 v120, v125
	s_add_i32 s7, s7, 16
	s_add_i32 s1, s1, 16
	s_add_i32 s12, s12, -16
	s_add_i32 s12, s12, -16
	s_cmp_lg_u32 s12, 0
	s_waitcnt lgkmcnt(0)
	s_lshl_b32 s1, s2, 11
	s_add_u32 s1, s23, s1
	ds_read2_b32 v[34:35], v3 offset0:33 offset1:41
	ds_read2_b32 v[46:47], v3 offset1:8
	ds_read2_b32 v[48:49], v3 offset0:66 offset1:74
	ds_read2_b32 v[50:51], v3 offset0:99 offset1:107
	ds_read2_b32 v[52:53], v3 offset0:132 offset1:140
	ds_read2_b32 v[54:55], v3 offset0:165 offset1:173
	ds_read2_b32 v[56:57], v3 offset0:198 offset1:206
	ds_read2_b32 v[58:59], v3 offset0:231 offset1:239
	s_addc_u32 s2, s24, 0
	s_lshl_b32 s0, s0, 1
	s_add_u32 s0, s1, s0
	s_addc_u32 s1, s2, 0
	v_lshlrev_b32_e32 v8, 1, v14
	v_lshl_add_u64 v[60:61], s[0:1], 0, v[8:9]
	s_waitcnt lgkmcnt(6)
	v_cvt_pk_bf16_f32 v42, v46, v34
	s_waitcnt lgkmcnt(4)
	v_cvt_pk_bf16_f32 v43, v48, v50
	s_waitcnt lgkmcnt(2)
	v_cvt_pk_bf16_f32 v44, v52, v54
	s_waitcnt lgkmcnt(0)
	v_cvt_pk_bf16_f32 v45, v56, v58
	v_lshl_add_u64 v[62:63], v[60:61], 0, v[24:25]
	global_store_dwordx4 v[62:63], v[42:45], off
	v_readlane_b32 s76, v254, 7
	v_readlane_b32 s83, v254, 6
	v_cvt_pk_bf16_f32 v42, v47, v35
	v_cvt_pk_bf16_f32 v43, v49, v51
	v_cvt_pk_bf16_f32 v44, v53, v55
	v_cvt_pk_bf16_f32 v45, v57, v59
	ds_read2_b32 v[46:47], v3 offset0:49 offset1:57
	ds_read2_b32 v[48:49], v3 offset0:16 offset1:24
	ds_read2_b32 v[50:51], v3 offset0:82 offset1:90
	ds_read2_b32 v[52:53], v3 offset0:115 offset1:123
	ds_read2_b32 v[54:55], v3 offset0:148 offset1:156
	ds_read2_b32 v[56:57], v3 offset0:181 offset1:189
	ds_read2_b32 v[58:59], v3 offset0:214 offset1:222
	ds_read2_b32 v[62:63], v3 offset0:247 offset1:255
	v_lshl_add_u64 v[34:35], v[60:61], 0, v[26:27]
	global_store_dwordx4 v[34:35], v[42:45], off
	v_lshl_add_u64 v[34:35], v[60:61], 0, v[28:29]
	v_readlane_b32 s77, v254, 8
	s_waitcnt lgkmcnt(6)
	v_cvt_pk_bf16_f32 v42, v48, v46
	s_waitcnt lgkmcnt(4)
	v_cvt_pk_bf16_f32 v43, v50, v52
	s_waitcnt lgkmcnt(2)
	v_cvt_pk_bf16_f32 v44, v54, v56
	s_waitcnt lgkmcnt(0)
	v_cvt_pk_bf16_f32 v45, v58, v62
	global_store_dwordx4 v[34:35], v[42:45], off
	v_lshl_add_u64 v[34:35], v[60:61], 0, v[30:31]
	s_nop 0
	v_cvt_pk_bf16_f32 v42, v49, v47
	v_cvt_pk_bf16_f32 v43, v51, v53
	v_cvt_pk_bf16_f32 v44, v55, v57
	v_cvt_pk_bf16_f32 v45, v59, v63
	global_store_dwordx4 v[34:35], v[42:45], off
	s_waitcnt lgkmcnt(0)

.LBB0_41:
	s_lshl_b32 s69, s1, 1
	s_lshl_b32 s70, s2, 1
	v_or_b32_e32 v8, s69, v1
	v_or_b32_e32 v33, s70, v6
	s_add_i32 s72, s69, 4
	s_add_i32 s73, s70, 4
	s_add_i32 s74, s69, 8
	s_add_i32 s75, s70, 8
	s_add_i32 s76, s69, 12
	s_add_i32 s77, s70, 12
	s_add_i32 s78, s69, 16
	s_add_i32 s79, s70, 16
	s_add_i32 s80, s69, 20
	s_add_i32 s81, s70, 20
	s_add_i32 s82, s69, 24
	s_add_i32 s83, s70, 24
	s_add_i32 s69, s69, 28
	s_add_i32 s84, s70, 28
	v_mad_u64_u32 v[42:43], s[70:71], v33, s67, v[34:35]
	v_or_b32_e32 v74, s72, v1
	v_or_b32_e32 v75, s73, v6
	v_or_b32_e32 v76, s74, v1
	v_or_b32_e32 v77, s75, v6
	v_or_b32_e32 v78, s76, v1
	v_or_b32_e32 v79, s77, v6
	v_or_b32_e32 v80, s78, v1
	v_or_b32_e32 v81, s79, v6
	v_or_b32_e32 v82, s80, v1
	v_or_b32_e32 v83, s81, v6
	v_or_b32_e32 v84, s82, v1
	v_or_b32_e32 v85, s83, v6
	v_or_b32_e32 v86, s69, v1
	v_or_b32_e32 v87, s84, v6
	v_mad_u64_u32 v[44:45], s[70:71], v8, s67, v[34:35]
	v_mad_u64_u32 v[46:47], s[70:71], v75, s67, v[34:35]
	v_mad_u64_u32 v[48:49], s[70:71], v74, s67, v[34:35]
	v_mad_u64_u32 v[50:51], s[70:71], v77, s67, v[34:35]
	v_mad_u64_u32 v[52:53], s[70:71], v76, s67, v[34:35]
	v_mad_u64_u32 v[54:55], s[70:71], v79, s67, v[34:35]
	v_mad_u64_u32 v[56:57], s[70:71], v78, s67, v[34:35]
	v_mad_u64_u32 v[58:59], s[70:71], v81, s67, v[34:35]
	v_mad_u64_u32 v[60:61], s[70:71], v80, s67, v[34:35]
	v_mad_u64_u32 v[62:63], s[70:71], v83, s67, v[34:35]
	v_mad_u64_u32 v[64:65], s[70:71], v82, s67, v[34:35]
	v_mad_u64_u32 v[66:67], s[70:71], v85, s67, v[34:35]
	v_mad_u64_u32 v[68:69], s[70:71], v84, s67, v[34:35]
	v_mad_u64_u32 v[70:71], s[70:71], v87, s67, v[34:35]
	v_mad_u64_u32 v[72:73], s[70:71], v86, s67, v[34:35]
	global_load_dword v88, v[42:43], off
	global_load_dword v89, v[44:45], off
	global_load_dword v90, v[46:47], off
	global_load_dword v91, v[48:49], off
	global_load_dword v92, v[50:51], off
	global_load_dword v93, v[52:53], off
	global_load_dword v94, v[54:55], off
	global_load_dword v95, v[56:57], off
	global_load_dword v96, v[58:59], off
	global_load_dword v97, v[60:61], off
	global_load_dword v98, v[62:63], off
	global_load_dword v99, v[64:65], off
	global_load_dword v100, v[66:67], off
	global_load_dword v101, v[68:69], off
	global_load_dword v102, v[70:71], off
	global_load_dword v103, v[72:73], off
	s_add_i32 s2, s2, 16
	s_add_i32 s1, s1, 16
	s_lshl_b32 s69, s1, 1
	s_lshl_b32 s70, s2, 1
	v_or_b32_e32 v136, s69, v1
	v_or_b32_e32 v137, s70, v6
	s_add_i32 s72, s69, 4
	s_add_i32 s73, s70, 4
	s_add_i32 s74, s69, 8
	s_add_i32 s75, s70, 8
	s_add_i32 s76, s69, 12
	s_add_i32 s77, s70, 12
	s_add_i32 s78, s69, 16
	s_add_i32 s79, s70, 16
	s_add_i32 s80, s69, 20
	s_add_i32 s81, s70, 20
	s_add_i32 s82, s69, 24
	s_add_i32 s83, s70, 24
	s_add_i32 s69, s69, 28
	s_add_i32 s84, s70, 28
	v_mad_u64_u32 v[104:105], s[70:71], v137, s67, v[34:35]
	v_or_b32_e32 v138, s72, v1
	v_or_b32_e32 v139, s73, v6
	v_or_b32_e32 v140, s74, v1
	v_or_b32_e32 v141, s75, v6
	v_or_b32_e32 v142, s76, v1
	v_or_b32_e32 v143, s77, v6
	v_or_b32_e32 v144, s78, v1
	v_or_b32_e32 v145, s79, v6
	v_or_b32_e32 v146, s80, v1
	v_or_b32_e32 v154, s81, v6
	v_or_b32_e32 v155, s82, v1
	v_or_b32_e32 v156, s83, v6
	v_or_b32_e32 v157, s69, v1
	v_or_b32_e32 v158, s84, v6
	v_mad_u64_u32 v[106:107], s[70:71], v136, s67, v[34:35]
	v_mad_u64_u32 v[108:109], s[70:71], v139, s67, v[34:35]
	v_mad_u64_u32 v[110:111], s[70:71], v138, s67, v[34:35]
	v_mad_u64_u32 v[112:113], s[70:71], v141, s67, v[34:35]
	v_mad_u64_u32 v[114:115], s[70:71], v140, s67, v[34:35]
	v_mad_u64_u32 v[116:117], s[70:71], v143, s67, v[34:35]
	v_mad_u64_u32 v[118:119], s[70:71], v142, s67, v[34:35]
	v_mad_u64_u32 v[120:121], s[70:71], v145, s67, v[34:35]
	v_mad_u64_u32 v[122:123], s[70:71], v144, s67, v[34:35]
	v_mad_u64_u32 v[124:125], s[70:71], v154, s67, v[34:35]
	v_mad_u64_u32 v[126:127], s[70:71], v146, s67, v[34:35]
	v_mad_u64_u32 v[128:129], s[70:71], v156, s67, v[34:35]
	v_mad_u64_u32 v[130:131], s[70:71], v155, s67, v[34:35]
	v_mad_u64_u32 v[132:133], s[70:71], v158, s67, v[34:35]
	v_mad_u64_u32 v[134:135], s[70:71], v157, s67, v[34:35]
	global_load_dword v159, v[104:105], off
	global_load_dword v160, v[106:107], off
	global_load_dword v161, v[108:109], off
	global_load_dword v162, v[110:111], off
	global_load_dword v163, v[112:113], off
	global_load_dword v164, v[114:115], off
	global_load_dword v165, v[116:117], off
	global_load_dword v166, v[118:119], off
	global_load_dword v167, v[120:121], off
	global_load_dword v168, v[122:123], off
	global_load_dword v169, v[124:125], off
	global_load_dword v170, v[126:127], off
	global_load_dword v171, v[128:129], off
	global_load_dword v172, v[130:131], off
	global_load_dword v173, v[132:133], off
	global_load_dword v174, v[134:135], off
	v_mad_u64_u32 v[42:43], s[70:71], v33, s31, v[12:13]
	v_mad_u64_u32 v[44:45], s[70:71], v8, s31, v[12:13]
	v_mad_u64_u32 v[46:47], s[70:71], v75, s31, v[12:13]
	v_mad_u64_u32 v[48:49], s[70:71], v74, s31, v[12:13]
	v_mad_u64_u32 v[50:51], s[70:71], v77, s31, v[12:13]
	v_mad_u64_u32 v[52:53], s[70:71], v76, s31, v[12:13]
	v_mad_u64_u32 v[54:55], s[70:71], v79, s31, v[12:13]
	v_mad_u64_u32 v[56:57], s[70:71], v78, s31, v[12:13]
	v_mad_u64_u32 v[58:59], s[70:71], v81, s31, v[12:13]
	v_mad_u64_u32 v[60:61], s[70:71], v80, s31, v[12:13]
	v_mad_u64_u32 v[62:63], s[70:71], v83, s31, v[12:13]
	v_mad_u64_u32 v[64:65], s[70:71], v82, s31, v[12:13]
	v_mad_u64_u32 v[66:67], s[70:71], v85, s31, v[12:13]
	v_mad_u64_u32 v[68:69], s[70:71], v84, s31, v[12:13]
	v_mad_u64_u32 v[70:71], s[70:71], v87, s31, v[12:13]
	v_mad_u64_u32 v[72:73], s[70:71], v86, s31, v[12:13]
	s_waitcnt vmcnt(31)
	ds_write_b32 v42, v88
	s_waitcnt vmcnt(30)
	ds_write_b32 v44, v89
	s_waitcnt vmcnt(29)
	ds_write_b32 v46, v90
	s_waitcnt vmcnt(28)
	ds_write_b32 v48, v91
	s_waitcnt vmcnt(27)
	ds_write_b32 v50, v92
	s_waitcnt vmcnt(26)
	ds_write_b32 v52, v93
	s_waitcnt vmcnt(25)
	ds_write_b32 v54, v94
	s_waitcnt vmcnt(24)
	ds_write_b32 v56, v95
	s_waitcnt vmcnt(23)
	ds_write_b32 v58, v96
	s_waitcnt vmcnt(22)
	ds_write_b32 v60, v97
	s_waitcnt vmcnt(21)
	ds_write_b32 v62, v98
	s_waitcnt vmcnt(20)
	ds_write_b32 v64, v99
	s_waitcnt vmcnt(19)
	ds_write_b32 v66, v100
	s_waitcnt vmcnt(18)
	ds_write_b32 v68, v101
	s_waitcnt vmcnt(17)
	ds_write_b32 v70, v102
	s_waitcnt vmcnt(16)
	ds_write_b32 v72, v103
	v_mad_u64_u32 v[104:105], s[70:71], v137, s31, v[12:13]
	v_mad_u64_u32 v[106:107], s[70:71], v136, s31, v[12:13]
	v_mad_u64_u32 v[108:109], s[70:71], v139, s31, v[12:13]
	v_mad_u64_u32 v[110:111], s[70:71], v138, s31, v[12:13]
	v_mad_u64_u32 v[112:113], s[70:71], v141, s31, v[12:13]
	v_mad_u64_u32 v[114:115], s[70:71], v140, s31, v[12:13]
	v_mad_u64_u32 v[116:117], s[70:71], v143, s31, v[12:13]
	v_mad_u64_u32 v[118:119], s[70:71], v142, s31, v[12:13]
	v_mad_u64_u32 v[120:121], s[70:71], v145, s31, v[12:13]
	v_mad_u64_u32 v[122:123], s[70:71], v144, s31, v[12:13]
	v_mad_u64_u32 v[124:125], s[70:71], v154, s31, v[12:13]
	v_mad_u64_u32 v[126:127], s[70:71], v146, s31, v[12:13]
	v_mad_u64_u32 v[128:129], s[70:71], v156, s31, v[12:13]
	v_mad_u64_u32 v[130:131], s[70:71], v155, s31, v[12:13]
	v_mad_u64_u32 v[132:133], s[70:71], v158, s31, v[12:13]
	v_mad_u64_u32 v[134:135], s[70:71], v157, s31, v[12:13]
	s_waitcnt vmcnt(15)
	ds_write_b32 v104, v159
	s_waitcnt vmcnt(14)
	ds_write_b32 v106, v160
	s_waitcnt vmcnt(13)
	ds_write_b32 v108, v161
	s_waitcnt vmcnt(12)
	ds_write_b32 v110, v162
	s_waitcnt vmcnt(11)
	ds_write_b32 v112, v163
	s_waitcnt vmcnt(10)
	ds_write_b32 v114, v164
	s_waitcnt vmcnt(9)
	ds_write_b32 v116, v165
	s_waitcnt vmcnt(8)
	ds_write_b32 v118, v166
	s_waitcnt vmcnt(7)
	ds_write_b32 v120, v167
	s_waitcnt vmcnt(6)
	ds_write_b32 v122, v168
	s_waitcnt vmcnt(5)
	ds_write_b32 v124, v169
	s_waitcnt vmcnt(4)
	ds_write_b32 v126, v170
	s_waitcnt vmcnt(3)
	ds_write_b32 v128, v171
	s_waitcnt vmcnt(2)
	ds_write_b32 v130, v172
	s_waitcnt vmcnt(1)
	ds_write_b32 v132, v173
	s_waitcnt vmcnt(0)
	ds_write_b32 v134, v174
	s_add_i32 s2, s2, 16
	s_add_i32 s1, s1, 16
	s_add_i32 s7, s7, -16
	s_add_i32 s7, s7, -16
	s_cmp_lg_u32 s7, 0
	s_sub_i32 s1, s6, 32
	s_cmp_lt_i32 s0, 48
	s_cselect_b32 s0, s6, s1
	s_ashr_i32 s1, s0, 31
	s_waitcnt lgkmcnt(0)
	s_lshl_b64 s[0:1], s[0:1], 11
	s_add_u32 s2, s28, s0
	ds_read2_b32 v[34:35], v3 offset0:33 offset1:41
	ds_read2_b32 v[46:47], v3 offset1:8
	ds_read2_b32 v[48:49], v3 offset0:66 offset1:74
	ds_read2_b32 v[50:51], v3 offset0:99 offset1:107
	ds_read2_b32 v[52:53], v3 offset0:132 offset1:140
	ds_read2_b32 v[54:55], v3 offset0:165 offset1:173
	ds_read2_b32 v[56:57], v3 offset0:198 offset1:206
	ds_read2_b32 v[58:59], v3 offset0:231 offset1:239
	s_addc_u32 s6, s29, s1
	s_lshl_b64 s[0:1], s[12:13], 1
	s_add_u32 s0, s2, s0
	s_addc_u32 s1, s6, s1
	v_lshlrev_b32_e32 v8, 1, v14
	v_lshl_add_u64 v[60:61], s[0:1], 0, v[8:9]
	s_waitcnt lgkmcnt(6)
	v_cvt_pk_bf16_f32 v42, v46, v34
	s_waitcnt lgkmcnt(4)
	v_cvt_pk_bf16_f32 v43, v48, v50
	s_waitcnt lgkmcnt(2)
	v_cvt_pk_bf16_f32 v44, v52, v54
	s_waitcnt lgkmcnt(0)
	v_cvt_pk_bf16_f32 v45, v56, v58
	v_lshl_add_u64 v[62:63], v[60:61], 0, v[24:25]
	global_store_dwordx4 v[62:63], v[42:45], off
	v_readlane_b32 s76, v254, 7
	s_mov_b32 s84, s85
	v_cvt_pk_bf16_f32 v42, v47, v35
	v_cvt_pk_bf16_f32 v43, v49, v51
	v_cvt_pk_bf16_f32 v44, v53, v55
	v_cvt_pk_bf16_f32 v45, v57, v59
	ds_read2_b32 v[46:47], v3 offset0:49 offset1:57
	ds_read2_b32 v[48:49], v3 offset0:16 offset1:24
	ds_read2_b32 v[50:51], v3 offset0:82 offset1:90
	ds_read2_b32 v[52:53], v3 offset0:115 offset1:123
	ds_read2_b32 v[54:55], v3 offset0:148 offset1:156
	ds_read2_b32 v[56:57], v3 offset0:181 offset1:189
	ds_read2_b32 v[58:59], v3 offset0:214 offset1:222
	ds_read2_b32 v[62:63], v3 offset0:247 offset1:255
	v_lshl_add_u64 v[34:35], v[60:61], 0, v[26:27]
	global_store_dwordx4 v[34:35], v[42:45], off
	v_lshl_add_u64 v[34:35], v[60:61], 0, v[28:29]
	v_readlane_b32 s83, v254, 6
	s_waitcnt lgkmcnt(6)
	v_cvt_pk_bf16_f32 v42, v48, v46
	s_waitcnt lgkmcnt(4)
	v_cvt_pk_bf16_f32 v43, v50, v52
	s_waitcnt lgkmcnt(2)
	v_cvt_pk_bf16_f32 v44, v54, v56
	s_waitcnt lgkmcnt(0)
	v_cvt_pk_bf16_f32 v45, v58, v62
	global_store_dwordx4 v[34:35], v[42:45], off
	v_lshl_add_u64 v[34:35], v[60:61], 0, v[30:31]
	v_readlane_b32 s77, v254, 8
	v_cvt_pk_bf16_f32 v42, v49, v47
	v_cvt_pk_bf16_f32 v43, v51, v53
	v_cvt_pk_bf16_f32 v44, v55, v57
	v_cvt_pk_bf16_f32 v45, v59, v63
	global_store_dwordx4 v[34:35], v[42:45], off
	s_waitcnt lgkmcnt(0)
	s_branch .LBB0_18
